# combine phase: 64-lane sum of squares by DPP and permlane swaps instead of six LDS permute round trips
# baseline (speedup 1.0000x reference)
; #define YB WSP(unsigned char, W_YB)
; __device__ __forceinline__ void combine_phase(LAS unsigned char* lds, const bf16_t* X, bf16_t* Xo, const unsigned char* __restrict__ YB, const float* __restrict__ mod_l, const int* __restrict__ cnt_l, ...
;     ...
;         for (int i = 0; i < 8; ++i) {
;             const int t = t0 + i;
;             u32x4 yv[4];
; #pragma unroll
;             for (int k = 0; k < 4; ++k) { const int row = __builtin_amdgcn_readlane(rowv, i * 4 + k); yv[k] = __builtin_nontemporal_load((const u32x4*)(YB + (size_t)row * D + k0)); }
;             const u32x4 x0 = *(const u32x4*)(X + (size_t)t * D + k0), x1 = *(const u32x4*)(X + (size_t)t * D + k0 + 8);
;             f32x4 v[4]; float ss = 0.f;
; #pragma unroll
;             for (int q = 0; q < 4; ++q) {
;                 f32x4 a = (f32x4){0.f, 0.f, 0.f, 0.f};
; #pragma unroll
;                 for (int k = 0; k < 4; ++k) { const unsigned w = q == 0 ? yv[k].x : q == 1 ? yv[k].y : q == 2 ? yv[k].z : yv[k].w;
;                     const f32x2_t lo = __builtin_amdgcn_cvt_pk_f32_fp8((int)w, false), hi = __builtin_amdgcn_cvt_pk_f32_fp8((int)w, true);
;                     a[0] += lo.x; a[1] += lo.y; a[2] += hi.x; a[3] += hi.y; }
.LBB0_1508:
	s_add_i32 s18, s21, -7
	v_readlane_b32 s18, v109, s18
	s_ashr_i32 s19, s18, 31
	s_lshl_b64 s[18:19], s[18:19], 10
	v_lshl_add_u64 v[52:53], v[72:73], 0, s[18:19]
	s_add_i32 s18, s21, -6
	v_readlane_b32 s18, v109, s18
	s_ashr_i32 s19, s18, 31
	s_lshl_b64 s[18:19], s[18:19], 10
	v_lshl_add_u64 v[56:57], v[72:73], 0, s[18:19]
	s_add_i32 s18, s21, -5
	v_readlane_b32 s18, v109, s18
	s_ashr_i32 s19, s18, 31
	s_lshl_b64 s[18:19], s[18:19], 10
	v_lshl_add_u64 v[60:61], v[72:73], 0, s[18:19]
	s_add_i32 s18, s21, -4
	v_readlane_b32 s18, v109, s18
	global_load_dwordx4 v[52:55], v[52:53], off nt
	s_ashr_i32 s19, s18, 31
	global_load_dwordx4 v[56:59], v[56:57], off nt
	s_lshl_b64 s[18:19], s[18:19], 10
	global_load_dwordx4 v[60:63], v[60:61], off nt
	v_lshl_add_u64 v[64:65], v[72:73], 0, s[18:19]
	global_load_dwordx4 v[64:67], v[64:65], off nt
	v_ashrrev_i32_e32 v99, 31, v98
	v_lshlrev_b64 v[68:69], 11, v[98:99]
	v_lshl_add_u64 v[102:103], v[74:75], 0, v[68:69]
	global_load_dwordx4 v[68:71], v[102:103], off offset:16
	global_load_dwordx4 v[110:113], v[102:103], off
	s_add_i32 s18, s21, -3
	v_readlane_b32 s18, v109, s18
	s_ashr_i32 s19, s18, 31
	s_lshl_b64 s[18:19], s[18:19], 10
	v_lshl_add_u64 v[182:183], v[72:73], 0, s[18:19]
	global_load_dwordx4 v[182:185], v[182:183], off nt
	s_add_i32 s18, s21, -2
	v_readlane_b32 s18, v109, s18
	s_ashr_i32 s19, s18, 31
	s_lshl_b64 s[18:19], s[18:19], 10
	v_lshl_add_u64 v[186:187], v[72:73], 0, s[18:19]
	global_load_dwordx4 v[186:189], v[186:187], off nt
	s_add_i32 s18, s21, -1
	v_readlane_b32 s18, v109, s18
	s_ashr_i32 s19, s18, 31
	s_lshl_b64 s[18:19], s[18:19], 10
	v_lshl_add_u64 v[190:191], v[72:73], 0, s[18:19]
	global_load_dwordx4 v[190:193], v[190:191], off nt
	v_readlane_b32 s18, v109, s21
	s_ashr_i32 s19, s18, 31
	s_lshl_b64 s[18:19], s[18:19], 10
	v_lshl_add_u64 v[194:195], v[72:73], 0, s[18:19]
	global_load_dwordx4 v[194:197], v[194:195], off nt
	v_add_u32_e32 v208, 1, v98
	v_ashrrev_i32_e32 v209, 31, v208
	v_lshlrev_b64 v[208:209], 11, v[208:209]
	v_lshl_add_u64 v[206:207], v[74:75], 0, v[208:209]
	global_load_dwordx4 v[198:201], v[206:207], off offset:16
	global_load_dwordx4 v[202:205], v[206:207], off
	s_mov_b32 s18, 0x358637bd
	v_lshlrev_b64 v[100:101], 10, v[98:99]
	s_waitcnt vmcnt(11)
	v_cvt_pk_f32_fp8_e32 v[102:103], v52
	v_cvt_pk_f32_fp8_sdwa v[104:105], v52 src0_sel:WORD_1
	s_waitcnt vmcnt(10)
	v_cvt_pk_f32_fp8_e32 v[114:115], v56
	v_cvt_pk_f32_fp8_sdwa v[116:117], v56 src0_sel:WORD_1
	s_waitcnt vmcnt(9)
	v_cvt_pk_f32_fp8_e32 v[118:119], v60
	v_cvt_pk_f32_fp8_sdwa v[120:121], v60 src0_sel:WORD_1
	s_waitcnt vmcnt(8)
	v_cvt_pk_f32_fp8_e32 v[122:123], v64
	v_cvt_pk_f32_fp8_sdwa v[124:125], v64 src0_sel:WORD_1
	v_pk_add_f32 v[104:105], v[104:105], 0 op_sel_hi:[1,0]
	v_pk_add_f32 v[102:103], v[102:103], 0 op_sel_hi:[1,0]
	v_pk_add_f32 v[104:105], v[104:105], v[116:117]
	v_pk_add_f32 v[102:103], v[102:103], v[114:115]
	v_pk_add_f32 v[104:105], v[104:105], v[120:121]
	v_pk_add_f32 v[102:103], v[102:103], v[118:119]
	v_cvt_pk_f32_fp8_e32 v[116:117], v61
	v_pk_add_f32 v[114:115], v[102:103], v[122:123]
	v_pk_add_f32 v[102:103], v[104:105], v[124:125]
	s_waitcnt vmcnt(6)
; __device__ __forceinline__ unsigned cvt_pk_bf16(float lo, float hi) { const bf16x2_t r = __builtin_convertvector((f32x2_t){lo, hi}, bf16x2_t); return __builtin_bit_cast(unsigned, r); }
; __device__ __forceinline__ float kf(float x) { asm volatile("" : "+s"(x)); return x; }
; __device__ __forceinline__ float shx(float v, int m) { int ln; asm volatile("v_mbcnt_lo_u32_b32 %0, -1, 0\n\tv_mbcnt_hi_u32_b32 %0, -1, %0" : "=v"(ln)); return __builtin_bit_cast(float, __builtin_amdgcn_ds_bpermute((ln ^ m) << 2, __builtin_bit_cast(int, v))); }
; __device__ __forceinline__ void combine_phase(LAS unsigned char* lds, const bf16_t* X, bf16_t* Xo, const unsigned char* __restrict__ YB, const float* __restrict__ mod_l, const int* __restrict__ cnt_l, ...
;     ...
;                 const u32x4 xq = (q >> 1) ? x1 : x0; const unsigned xa = (q & 1) ? xq.z : xq.x, xb = (q & 1) ? xq.w : xq.y;
;                 v[q] = (f32x4){__uint_as_float(xa << 16), __uint_as_float(xa & 0xffff0000u), __uint_as_float(xb << 16), __uint_as_float(xb & 0xffff0000u)} + g2[q] * a;
;                 ss += v[q][0] * v[q][0] + v[q][1] * v[q][1] + v[q][2] * v[q][2] + v[q][3] * v[q][3];
;             }
;             for (int of = 32; of > 0; of >>= 1) ss += shx(ss, of);
;             const float r = rsqrtf(ss * (1.f / D) + kf(EPS));
;             if (mod_n) {
;                 u32x4 xo0, xo1, h0, h1;
;                 xo0.x = cvt_pk_bf16(v[0][0], v[0][1]); xo0.y = cvt_pk_bf16(v[0][2], v[0][3]); xo0.z = cvt_pk_bf16(v[1][0], v[1][1]); xo0.w = cvt_pk_bf16(v[1][2], v[1][3]);
;                 xo1.x = cvt_pk_bf16(v[2][0], v[2][1]); xo1.y = cvt_pk_bf16(v[2][2], v[2][3]); xo1.z = cvt_pk_bf16(v[3][0], v[3][1]); xo1.w = cvt_pk_bf16(v[3][2], v[3][3]);
;                 *(u32x4*)(Xo + (size_t)t * D + k0) = xo0; *(u32x4*)(Xo + (size_t)t * D + k0 + 8) = xo1;
;                 f32x4 o[4];
; #pragma unroll
;                 for (int q = 0; q < 4; ++q) o[q] = v[q] * r * gn[q] + sh[q];
;                 h0.x = cvt_pk_bf16(o[0][0], o[0][1]); h0.y = cvt_pk_bf16(o[0][2], o[0][3]); h0.z = cvt_pk_bf16(o[1][0], o[1][1]); h0.w = cvt_pk_bf16(o[1][2], o[1][3]);
;                 h1.x = cvt_pk_bf16(o[2][0], o[2][1]); h1.y = cvt_pk_bf16(o[2][2], o[2][3]); h1.z = cvt_pk_bf16(o[3][0], o[3][1]); h1.w = cvt_pk_bf16(o[3][2], o[3][3]);
;                 *(u32x4*)(H1B + (size_t)t * D + k0) = h0; *(u32x4*)(H1B + (size_t)t * D + k0 + 8) = h1;
	v_lshlrev_b32_e32 v104, 16, v110
	v_and_b32_e32 v105, 0xffff0000, v110
	v_lshlrev_b32_e32 v110, 16, v111
	v_and_b32_e32 v111, 0xffff0000, v111
	v_pk_fma_f32 v[102:103], v[94:95], v[102:103], v[110:111]
	v_cvt_pk_f32_fp8_e32 v[110:111], v53
	v_pk_fma_f32 v[104:105], v[96:97], v[114:115], v[104:105]
	v_cvt_pk_f32_fp8_sdwa v[52:53], v53 src0_sel:WORD_1
	v_cvt_pk_f32_fp8_e32 v[114:115], v57
	v_cvt_pk_f32_fp8_sdwa v[56:57], v57 src0_sel:WORD_1
	v_cvt_pk_f32_fp8_sdwa v[60:61], v61 src0_sel:WORD_1
	v_cvt_pk_f32_fp8_e32 v[118:119], v65
	v_cvt_pk_f32_fp8_sdwa v[64:65], v65 src0_sel:WORD_1
	v_pk_add_f32 v[110:111], v[110:111], 0 op_sel_hi:[1,0]
	v_pk_add_f32 v[52:53], v[52:53], 0 op_sel_hi:[1,0]
	v_pk_add_f32 v[110:111], v[110:111], v[114:115]
	v_pk_add_f32 v[52:53], v[52:53], v[56:57]
	v_pk_add_f32 v[56:57], v[110:111], v[116:117]
	v_pk_add_f32 v[52:53], v[52:53], v[60:61]
	v_pk_add_f32 v[56:57], v[56:57], v[118:119]
	v_lshlrev_b32_e32 v60, 16, v112
	v_and_b32_e32 v61, 0xffff0000, v112
	v_pk_add_f32 v[52:53], v[52:53], v[64:65]
	v_lshlrev_b32_e32 v64, 16, v113
	v_and_b32_e32 v65, 0xffff0000, v113
	v_pk_fma_f32 v[56:57], v[92:93], v[56:57], v[60:61]
	v_pk_fma_f32 v[52:53], v[90:91], v[52:53], v[64:65]
	v_mov_b32_e32 v64, v105
	v_mov_b32_e32 v65, v57
	v_mov_b32_e32 v60, v104
	v_mov_b32_e32 v61, v56
	v_pk_mul_f32 v[64:65], v[64:65], v[64:65]
	v_cvt_pk_f32_fp8_sdwa v[110:111], v54 src0_sel:WORD_1
	v_pk_fma_f32 v[60:61], v[60:61], v[60:61], v[64:65]
	v_mov_b32_e32 v64, v102
	v_mov_b32_e32 v65, v52
	v_pk_fma_f32 v[60:61], v[64:65], v[64:65], v[60:61]
	v_mov_b32_e32 v64, v103
	v_mov_b32_e32 v65, v53
	v_pk_fma_f32 v[60:61], v[64:65], v[64:65], v[60:61]
	v_cvt_pk_f32_fp8_e32 v[64:65], v54
	v_cvt_pk_f32_fp8_e32 v[112:113], v58
	v_cvt_pk_f32_fp8_sdwa v[114:115], v58 src0_sel:WORD_1
	v_cvt_pk_f32_fp8_e32 v[116:117], v62
	v_cvt_pk_f32_fp8_sdwa v[118:119], v62 src0_sel:WORD_1
	v_cvt_pk_f32_fp8_e32 v[120:121], v66
	v_cvt_pk_f32_fp8_sdwa v[122:123], v66 src0_sel:WORD_1
	v_pk_add_f32 v[110:111], v[110:111], 0 op_sel_hi:[1,0]
	v_pk_add_f32 v[64:65], v[64:65], 0 op_sel_hi:[1,0]
	v_pk_add_f32 v[110:111], v[110:111], v[114:115]
	v_pk_add_f32 v[64:65], v[64:65], v[112:113]
	v_pk_add_f32 v[110:111], v[110:111], v[118:119]
	v_pk_add_f32 v[64:65], v[64:65], v[116:117]
	v_cvt_pk_f32_fp8_e32 v[114:115], v63
	v_pk_add_f32 v[112:113], v[64:65], v[120:121]
	v_pk_add_f32 v[64:65], v[110:111], v[122:123]
	v_lshlrev_b32_e32 v110, 16, v68
	v_and_b32_e32 v111, 0xffff0000, v68
	v_lshlrev_b32_e32 v68, 16, v69
	v_and_b32_e32 v69, 0xffff0000, v69
	v_pk_fma_f32 v[64:65], v[86:87], v[64:65], v[68:69]
	v_pk_fma_f32 v[68:69], v[88:89], v[112:113], v[110:111]
	v_cvt_pk_f32_fp8_e32 v[110:111], v55
	v_cvt_pk_f32_fp8_sdwa v[54:55], v55 src0_sel:WORD_1
	v_cvt_pk_f32_fp8_e32 v[112:113], v59
	v_cvt_pk_f32_fp8_sdwa v[58:59], v59 src0_sel:WORD_1
	v_cvt_pk_f32_fp8_sdwa v[62:63], v63 src0_sel:WORD_1
	v_cvt_pk_f32_fp8_e32 v[116:117], v67
	v_cvt_pk_f32_fp8_sdwa v[66:67], v67 src0_sel:WORD_1
	v_pk_add_f32 v[110:111], v[110:111], 0 op_sel_hi:[1,0]
	v_pk_add_f32 v[54:55], v[54:55], 0 op_sel_hi:[1,0]
	v_pk_add_f32 v[110:111], v[110:111], v[112:113]
	v_pk_add_f32 v[54:55], v[54:55], v[58:59]
	v_pk_add_f32 v[58:59], v[110:111], v[114:115]
	v_pk_add_f32 v[54:55], v[54:55], v[62:63]
	v_pk_add_f32 v[58:59], v[58:59], v[116:117]
	v_lshlrev_b32_e32 v62, 16, v70
	v_and_b32_e32 v63, 0xffff0000, v70
	v_pk_add_f32 v[54:55], v[54:55], v[66:67]
	v_lshlrev_b32_e32 v66, 16, v71
	v_and_b32_e32 v67, 0xffff0000, v71
	v_pk_fma_f32 v[58:59], v[84:85], v[58:59], v[62:63]
	v_pk_fma_f32 v[54:55], v[82:83], v[54:55], v[66:67]
	v_mov_b32_e32 v66, v69
	v_mov_b32_e32 v67, v59
	v_mov_b32_e32 v62, v68
	v_mov_b32_e32 v63, v58
	v_pk_mul_f32 v[66:67], v[66:67], v[66:67]
	v_add_f32_e32 v60, v60, v61
	v_pk_fma_f32 v[62:63], v[62:63], v[62:63], v[66:67]
	v_mov_b32_e32 v66, v64
	v_mov_b32_e32 v67, v54
	v_pk_fma_f32 v[62:63], v[66:67], v[66:67], v[62:63]
	v_mov_b32_e32 v66, v65
	v_mov_b32_e32 v67, v55
	v_pk_fma_f32 v[62:63], v[66:67], v[66:67], v[62:63]
	v_add_f32_e32 v60, v60, v62
	v_add_f32_e32 v60, v60, v63
	s_nop 1
	v_add_f32_dpp v60, v60, v60 quad_perm:[1,0,3,2] row_mask:0xf bank_mask:0xf
	s_nop 1
	v_add_f32_dpp v60, v60, v60 quad_perm:[2,3,0,1] row_mask:0xf bank_mask:0xf
	s_nop 1
	v_add_f32_dpp v60, v60, v60 row_half_mirror row_mask:0xf bank_mask:0xf
	s_nop 1
	v_add_f32_dpp v60, v60, v60 row_mirror row_mask:0xf bank_mask:0xf
	v_mov_b32_e32 v61, v60
	s_nop 1
	v_permlane16_swap_b32_e32 v60, v61
	v_add_f32_e32 v60, v60, v61
	v_mov_b32_e32 v61, v60
	s_nop 1
	v_permlane32_swap_b32_e32 v60, v61
	v_add_f32_e32 v60, v60, v61
	v_mov_b32_e32 v61, s18
	v_fmac_f32_e32 v61, 0x3a800000, v60
	v_cmp_gt_f32_e32 vcc, s80, v61
	v_mul_f32_e32 v60, 0x4b800000, v61
	s_nop 0
	v_cndmask_b32_e32 v60, v61, v60, vcc
	v_rsq_f32_e32 v60, v60
	s_nop 0
	v_mul_f32_e32 v61, 0x45800000, v60
	v_cndmask_b32_e32 v60, v60, v61, vcc
	s_and_b64 vcc, exec, s[16:17]
	s_cbranch_vccz .LBB0_1513
	v_lshlrev_b64 v[62:63], 1, v[100:101]
	v_cvt_pk_bf16_f32 v110, v104, v105
	v_cvt_pk_bf16_f32 v111, v102, v103
	v_cvt_pk_bf16_f32 v112, v56, v57
	v_cvt_pk_bf16_f32 v113, v52, v53
	v_lshl_add_u64 v[66:67], v[76:77], 0, v[62:63]
	v_cvt_pk_bf16_f32 v114, v68, v69
	v_cvt_pk_bf16_f32 v115, v64, v65
	v_cvt_pk_bf16_f32 v116, v58, v59
	v_cvt_pk_bf16_f32 v117, v54, v55
	global_store_dwordx4 v[66:67], v[110:113], off
	global_store_dwordx4 v[66:67], v[114:117], off offset:16
	v_pk_mul_f32 v[66:67], v[102:103], v[60:61] op_sel_hi:[1,0]
	v_pk_mul_f32 v[110:111], v[52:53], v[60:61] op_sel_hi:[1,0]
	v_pk_mul_f32 v[70:71], v[104:105], v[60:61] op_sel_hi:[1,0]
	v_pk_mul_f32 v[112:113], v[56:57], v[60:61] op_sel_hi:[1,0]
	v_pk_fma_f32 v[114:115], v[32:33], v[110:111], v[20:21]
	v_pk_mul_f32 v[110:111], v[64:65], v[60:61] op_sel_hi:[1,0]
	v_pk_fma_f32 v[66:67], v[28:29], v[66:67], v[24:25]
	v_pk_fma_f32 v[70:71], v[26:27], v[70:71], v[22:23]
	v_pk_fma_f32 v[112:113], v[30:31], v[112:113], v[18:19]
	v_pk_mul_f32 v[116:117], v[68:69], v[60:61] op_sel_hi:[1,0]
	v_pk_fma_f32 v[118:119], v[46:47], v[110:111], v[42:43]
	v_pk_mul_f32 v[110:111], v[54:55], v[60:61] op_sel_hi:[1,0]
	v_pk_mul_f32 v[120:121], v[58:59], v[60:61] op_sel_hi:[1,0]
	v_pk_fma_f32 v[116:117], v[44:45], v[116:117], v[40:41]
	v_pk_fma_f32 v[122:123], v[50:51], v[110:111], v[38:39]
	v_pk_fma_f32 v[120:121], v[48:49], v[120:121], v[36:37]
	v_cvt_pk_bf16_f32 v110, v70, v71
	v_cvt_pk_bf16_f32 v111, v66, v67
	v_cvt_pk_bf16_f32 v112, v112, v113
	v_cvt_pk_bf16_f32 v113, v114, v115
	v_lshl_add_u64 v[62:63], v[78:79], 0, v[62:63]
	v_cvt_pk_bf16_f32 v114, v116, v117
	v_cvt_pk_bf16_f32 v115, v118, v119
	v_cvt_pk_bf16_f32 v116, v120, v121
	v_cvt_pk_bf16_f32 v117, v122, v123
	global_store_dwordx4 v[62:63], v[110:113], off
	global_store_dwordx4 v[62:63], v[114:117], off offset:16
	s_cbranch_execnz .LBB0_1511

; __device__ __forceinline__ float kf(float x) { asm volatile("" : "+s"(x)); return x; }
; __device__ __forceinline__ float shx(float v, int m) { int ln; asm volatile("v_mbcnt_lo_u32_b32 %0, -1, 0\n\tv_mbcnt_hi_u32_b32 %0, -1, %0" : "=v"(ln)); return __builtin_bit_cast(float, __builtin_amdgcn_ds_bpermute((ln ^ m) << 2, __builtin_bit_cast(int, v))); }
; #define YB WSP(unsigned char, W_YB)
; __device__ __forceinline__ void combine_phase(LAS unsigned char* lds, const bf16_t* X, bf16_t* Xo, const unsigned char* __restrict__ YB, const float* __restrict__ mod_l, const int* __restrict__ cnt_l, ...
;     ...
;             for (int k = 0; k < 4; ++k) { const int row = __builtin_amdgcn_readlane(rowv, i * 4 + k); yv[k] = __builtin_nontemporal_load((const u32x4*)(YB + (size_t)row * D + k0)); }
;             const u32x4 x0 = *(const u32x4*)(X + (size_t)t * D + k0), x1 = *(const u32x4*)(X + (size_t)t * D + k0 + 8);
;             f32x4 v[4]; float ss = 0.f;
; #pragma unroll
;             for (int q = 0; q < 4; ++q) {
;                 f32x4 a = (f32x4){0.f, 0.f, 0.f, 0.f};
; #pragma unroll
;                 for (int k = 0; k < 4; ++k) { const unsigned w = q == 0 ? yv[k].x : q == 1 ? yv[k].y : q == 2 ? yv[k].z : yv[k].w;
;                     const f32x2_t lo = __builtin_amdgcn_cvt_pk_f32_fp8((int)w, false), hi = __builtin_amdgcn_cvt_pk_f32_fp8((int)w, true);
;                     a[0] += lo.x; a[1] += lo.y; a[2] += hi.x; a[3] += hi.y; }
;                 const u32x4 xq = (q >> 1) ? x1 : x0; const unsigned xa = (q & 1) ? xq.z : xq.x, xb = (q & 1) ? xq.w : xq.y;
;                 v[q] = (f32x4){__uint_as_float(xa << 16), __uint_as_float(xa & 0xffff0000u), __uint_as_float(xb << 16), __uint_as_float(xb & 0xffff0000u)} + g2[q] * a;
;                 ss += v[q][0] * v[q][0] + v[q][1] * v[q][1] + v[q][2] * v[q][2] + v[q][3] * v[q][3];
;             }
;             for (int of = 32; of > 0; of >>= 1) ss += shx(ss, of);
;             const float r = rsqrtf(ss * (1.f / D) + kf(EPS));
.LBB0_1511:
	v_add_u32_e32 v68, 1, v98
	v_ashrrev_i32_e32 v69, 31, v68
	v_lshlrev_b64 v[100:101], 10, v[68:69]
	s_mov_b32 s18, 0x358637bd
	s_waitcnt vmcnt(9)
	v_cvt_pk_f32_fp8_e32 v[102:103], v182
	v_cvt_pk_f32_fp8_sdwa v[104:105], v182 src0_sel:WORD_1
	s_waitcnt vmcnt(8)
	v_cvt_pk_f32_fp8_e32 v[114:115], v186
	v_cvt_pk_f32_fp8_sdwa v[116:117], v186 src0_sel:WORD_1
	s_waitcnt vmcnt(7)
	v_cvt_pk_f32_fp8_e32 v[118:119], v190
	v_cvt_pk_f32_fp8_sdwa v[120:121], v190 src0_sel:WORD_1
	s_waitcnt vmcnt(6)
	v_cvt_pk_f32_fp8_e32 v[122:123], v194
	v_cvt_pk_f32_fp8_sdwa v[124:125], v194 src0_sel:WORD_1
	v_pk_add_f32 v[104:105], v[104:105], 0 op_sel_hi:[1,0]
	v_pk_add_f32 v[102:103], v[102:103], 0 op_sel_hi:[1,0]
	v_pk_add_f32 v[104:105], v[104:105], v[116:117]
	v_pk_add_f32 v[102:103], v[102:103], v[114:115]
	v_pk_add_f32 v[104:105], v[104:105], v[120:121]
	v_pk_add_f32 v[102:103], v[102:103], v[118:119]
	v_cvt_pk_f32_fp8_e32 v[116:117], v191
	v_pk_add_f32 v[114:115], v[102:103], v[122:123]
	v_pk_add_f32 v[102:103], v[104:105], v[124:125]
	s_waitcnt vmcnt(4)
	v_lshlrev_b32_e32 v104, 16, v202
	v_and_b32_e32 v105, 0xffff0000, v202
	v_lshlrev_b32_e32 v110, 16, v203
	v_and_b32_e32 v111, 0xffff0000, v203
	v_pk_fma_f32 v[102:103], v[94:95], v[102:103], v[110:111]
	v_cvt_pk_f32_fp8_e32 v[110:111], v183
	v_pk_fma_f32 v[104:105], v[96:97], v[114:115], v[104:105]
	v_cvt_pk_f32_fp8_sdwa v[52:53], v183 src0_sel:WORD_1
	v_cvt_pk_f32_fp8_e32 v[114:115], v187
	v_cvt_pk_f32_fp8_sdwa v[56:57], v187 src0_sel:WORD_1
	v_cvt_pk_f32_fp8_sdwa v[60:61], v191 src0_sel:WORD_1
	v_cvt_pk_f32_fp8_e32 v[118:119], v195
	v_cvt_pk_f32_fp8_sdwa v[64:65], v195 src0_sel:WORD_1
	v_pk_add_f32 v[110:111], v[110:111], 0 op_sel_hi:[1,0]
	v_pk_add_f32 v[52:53], v[52:53], 0 op_sel_hi:[1,0]
	v_pk_add_f32 v[110:111], v[110:111], v[114:115]
	v_pk_add_f32 v[52:53], v[52:53], v[56:57]
	v_pk_add_f32 v[56:57], v[110:111], v[116:117]
	v_pk_add_f32 v[52:53], v[52:53], v[60:61]
	v_pk_add_f32 v[56:57], v[56:57], v[118:119]
	v_lshlrev_b32_e32 v60, 16, v204
	v_and_b32_e32 v61, 0xffff0000, v204
	v_pk_add_f32 v[52:53], v[52:53], v[64:65]
	v_lshlrev_b32_e32 v64, 16, v205
	v_and_b32_e32 v65, 0xffff0000, v205
	v_pk_fma_f32 v[56:57], v[92:93], v[56:57], v[60:61]
	v_pk_fma_f32 v[52:53], v[90:91], v[52:53], v[64:65]
	v_mov_b32_e32 v64, v105
	v_mov_b32_e32 v65, v57
	v_mov_b32_e32 v60, v104
	v_mov_b32_e32 v61, v56
	v_pk_mul_f32 v[64:65], v[64:65], v[64:65]
	v_cvt_pk_f32_fp8_sdwa v[110:111], v184 src0_sel:WORD_1
	v_pk_fma_f32 v[60:61], v[60:61], v[60:61], v[64:65]
	v_mov_b32_e32 v64, v102
	v_mov_b32_e32 v65, v52
	v_pk_fma_f32 v[60:61], v[64:65], v[64:65], v[60:61]
	v_mov_b32_e32 v64, v103
	v_mov_b32_e32 v65, v53
	v_pk_fma_f32 v[60:61], v[64:65], v[64:65], v[60:61]
	v_cvt_pk_f32_fp8_e32 v[64:65], v184
	v_cvt_pk_f32_fp8_e32 v[112:113], v188
	v_cvt_pk_f32_fp8_sdwa v[114:115], v188 src0_sel:WORD_1
	v_cvt_pk_f32_fp8_e32 v[116:117], v192
	v_cvt_pk_f32_fp8_sdwa v[118:119], v192 src0_sel:WORD_1
	v_cvt_pk_f32_fp8_e32 v[120:121], v196
	v_cvt_pk_f32_fp8_sdwa v[122:123], v196 src0_sel:WORD_1
	v_pk_add_f32 v[110:111], v[110:111], 0 op_sel_hi:[1,0]
	v_pk_add_f32 v[64:65], v[64:65], 0 op_sel_hi:[1,0]
	v_pk_add_f32 v[110:111], v[110:111], v[114:115]
	v_pk_add_f32 v[64:65], v[64:65], v[112:113]
	v_pk_add_f32 v[110:111], v[110:111], v[118:119]
	v_pk_add_f32 v[64:65], v[64:65], v[116:117]
	v_cvt_pk_f32_fp8_e32 v[114:115], v193
	v_pk_add_f32 v[112:113], v[64:65], v[120:121]
	v_pk_add_f32 v[64:65], v[110:111], v[122:123]
	v_lshlrev_b32_e32 v110, 16, v198
	v_and_b32_e32 v111, 0xffff0000, v198
	v_lshlrev_b32_e32 v68, 16, v199
	v_and_b32_e32 v69, 0xffff0000, v199
	v_pk_fma_f32 v[64:65], v[86:87], v[64:65], v[68:69]
	v_pk_fma_f32 v[68:69], v[88:89], v[112:113], v[110:111]
	v_cvt_pk_f32_fp8_e32 v[110:111], v185
	v_cvt_pk_f32_fp8_sdwa v[54:55], v185 src0_sel:WORD_1
	v_cvt_pk_f32_fp8_e32 v[112:113], v189
	v_cvt_pk_f32_fp8_sdwa v[58:59], v189 src0_sel:WORD_1
	v_cvt_pk_f32_fp8_sdwa v[62:63], v193 src0_sel:WORD_1
	v_cvt_pk_f32_fp8_e32 v[116:117], v197
	v_cvt_pk_f32_fp8_sdwa v[66:67], v197 src0_sel:WORD_1
	v_pk_add_f32 v[110:111], v[110:111], 0 op_sel_hi:[1,0]
	v_pk_add_f32 v[54:55], v[54:55], 0 op_sel_hi:[1,0]
	v_pk_add_f32 v[110:111], v[110:111], v[112:113]
	v_pk_add_f32 v[54:55], v[54:55], v[58:59]
	v_pk_add_f32 v[58:59], v[110:111], v[114:115]
	v_pk_add_f32 v[54:55], v[54:55], v[62:63]
	v_pk_add_f32 v[58:59], v[58:59], v[116:117]
	v_lshlrev_b32_e32 v62, 16, v200
	v_and_b32_e32 v63, 0xffff0000, v200
	v_pk_add_f32 v[54:55], v[54:55], v[66:67]
	v_lshlrev_b32_e32 v66, 16, v201
	v_and_b32_e32 v67, 0xffff0000, v201
	v_pk_fma_f32 v[58:59], v[84:85], v[58:59], v[62:63]
	v_pk_fma_f32 v[54:55], v[82:83], v[54:55], v[66:67]
	v_mov_b32_e32 v66, v69
	v_mov_b32_e32 v67, v59
	v_mov_b32_e32 v62, v68
	v_mov_b32_e32 v63, v58
	v_pk_mul_f32 v[66:67], v[66:67], v[66:67]
	v_add_f32_e32 v60, v60, v61
	v_pk_fma_f32 v[62:63], v[62:63], v[62:63], v[66:67]
	v_mov_b32_e32 v66, v64
	v_mov_b32_e32 v67, v54
	v_pk_fma_f32 v[62:63], v[66:67], v[66:67], v[62:63]
	v_mov_b32_e32 v66, v65
	v_mov_b32_e32 v67, v55
	v_pk_fma_f32 v[62:63], v[66:67], v[66:67], v[62:63]
	v_add_f32_e32 v60, v60, v62
	v_add_f32_e32 v60, v60, v63
	s_nop 1
	v_add_f32_dpp v60, v60, v60 quad_perm:[1,0,3,2] row_mask:0xf bank_mask:0xf
	s_nop 1
	v_add_f32_dpp v60, v60, v60 quad_perm:[2,3,0,1] row_mask:0xf bank_mask:0xf
	s_nop 1
	v_add_f32_dpp v60, v60, v60 row_half_mirror row_mask:0xf bank_mask:0xf
	s_nop 1
	v_add_f32_dpp v60, v60, v60 row_mirror row_mask:0xf bank_mask:0xf
	v_mov_b32_e32 v61, v60
	s_nop 1
	v_permlane16_swap_b32_e32 v60, v61
	v_add_f32_e32 v60, v60, v61
	v_mov_b32_e32 v61, v60
	s_nop 1
	v_permlane32_swap_b32_e32 v60, v61
	v_add_f32_e32 v60, v60, v61
	v_mov_b32_e32 v61, s18
	v_fmac_f32_e32 v61, 0x3a800000, v60
	v_cmp_gt_f32_e32 vcc, s80, v61
	v_mul_f32_e32 v60, 0x4b800000, v61
	s_nop 0
	v_cndmask_b32_e32 v60, v61, v60, vcc
	v_rsq_f32_e32 v60, v60
	s_nop 0
	v_mul_f32_e32 v61, 0x45800000, v60
	v_cndmask_b32_e32 v60, v60, v61, vcc
	s_and_b64 vcc, exec, s[6:7]
	s_cbranch_vccnz .LBB0_1514
; __device__ __forceinline__ unsigned cvt_pk_bf16(float lo, float hi) { const bf16x2_t r = __builtin_convertvector((f32x2_t){lo, hi}, bf16x2_t); return __builtin_bit_cast(unsigned, r); }
; __device__ __forceinline__ void combine_phase(LAS unsigned char* lds, const bf16_t* X, bf16_t* Xo, const unsigned char* __restrict__ YB, const float* __restrict__ mod_l, const int* __restrict__ cnt_l, ...
;     ...
;                 u32x4 xo0, xo1, h0, h1;
;                 xo0.x = cvt_pk_bf16(v[0][0], v[0][1]); xo0.y = cvt_pk_bf16(v[0][2], v[0][3]); xo0.z = cvt_pk_bf16(v[1][0], v[1][1]); xo0.w = cvt_pk_bf16(v[1][2], v[1][3]);
;                 xo1.x = cvt_pk_bf16(v[2][0], v[2][1]); xo1.y = cvt_pk_bf16(v[2][2], v[2][3]); xo1.z = cvt_pk_bf16(v[3][0], v[3][1]); xo1.w = cvt_pk_bf16(v[3][2], v[3][3]);
;                 *(u32x4*)(Xo + (size_t)t * D + k0) = xo0; *(u32x4*)(Xo + (size_t)t * D + k0 + 8) = xo1;
;                 f32x4 o[4];
; #pragma unroll
;                 for (int q = 0; q < 4; ++q) o[q] = v[q] * r * gn[q] + sh[q];
;                 h0.x = cvt_pk_bf16(o[0][0], o[0][1]); h0.y = cvt_pk_bf16(o[0][2], o[0][3]); h0.z = cvt_pk_bf16(o[1][0], o[1][1]); h0.w = cvt_pk_bf16(o[1][2], o[1][3]);
;                 h1.x = cvt_pk_bf16(o[2][0], o[2][1]); h1.y = cvt_pk_bf16(o[2][2], o[2][3]); h1.z = cvt_pk_bf16(o[3][0], o[3][1]); h1.w = cvt_pk_bf16(o[3][2], o[3][3]);
;                 *(u32x4*)(H1B + (size_t)t * D + k0) = h0; *(u32x4*)(H1B + (size_t)t * D + k0 + 8) = h1;
	v_lshlrev_b64 v[62:63], 1, v[100:101]
	v_cvt_pk_bf16_f32 v110, v104, v105
	v_cvt_pk_bf16_f32 v111, v102, v103
	v_cvt_pk_bf16_f32 v112, v56, v57
	v_cvt_pk_bf16_f32 v113, v52, v53
	v_lshl_add_u64 v[66:67], v[76:77], 0, v[62:63]
	v_cvt_pk_bf16_f32 v114, v68, v69
	v_cvt_pk_bf16_f32 v115, v64, v65
	v_cvt_pk_bf16_f32 v116, v58, v59
	v_cvt_pk_bf16_f32 v117, v54, v55
	global_store_dwordx4 v[66:67], v[110:113], off
	global_store_dwordx4 v[66:67], v[114:117], off offset:16
	v_pk_mul_f32 v[66:67], v[102:103], v[60:61] op_sel_hi:[1,0]
	v_pk_mul_f32 v[110:111], v[52:53], v[60:61] op_sel_hi:[1,0]
	v_pk_mul_f32 v[70:71], v[104:105], v[60:61] op_sel_hi:[1,0]
	v_pk_mul_f32 v[112:113], v[56:57], v[60:61] op_sel_hi:[1,0]
	v_pk_fma_f32 v[114:115], v[32:33], v[110:111], v[20:21]
	v_pk_mul_f32 v[110:111], v[64:65], v[60:61] op_sel_hi:[1,0]
	v_pk_fma_f32 v[66:67], v[28:29], v[66:67], v[24:25]
	v_pk_fma_f32 v[70:71], v[26:27], v[70:71], v[22:23]
	v_pk_fma_f32 v[112:113], v[30:31], v[112:113], v[18:19]
	v_pk_mul_f32 v[116:117], v[68:69], v[60:61] op_sel_hi:[1,0]
	v_pk_fma_f32 v[118:119], v[46:47], v[110:111], v[42:43]
	v_pk_mul_f32 v[110:111], v[54:55], v[60:61] op_sel_hi:[1,0]
	v_pk_mul_f32 v[120:121], v[58:59], v[60:61] op_sel_hi:[1,0]
	v_pk_fma_f32 v[116:117], v[44:45], v[116:117], v[40:41]
	v_pk_fma_f32 v[122:123], v[50:51], v[110:111], v[38:39]
	v_pk_fma_f32 v[120:121], v[48:49], v[120:121], v[36:37]
	v_cvt_pk_bf16_f32 v110, v70, v71
	v_cvt_pk_bf16_f32 v111, v66, v67
	v_cvt_pk_bf16_f32 v112, v112, v113
	v_cvt_pk_bf16_f32 v113, v114, v115
	v_lshl_add_u64 v[62:63], v[78:79], 0, v[62:63]
	v_cvt_pk_bf16_f32 v114, v116, v117
	v_cvt_pk_bf16_f32 v115, v118, v119
	v_cvt_pk_bf16_f32 v116, v120, v121
	v_cvt_pk_bf16_f32 v117, v122, v123
	global_store_dwordx4 v[62:63], v[110:113], off
	global_store_dwordx4 v[62:63], v[114:117], off offset:16
	s_cbranch_execnz .LBB0_1507
	s_branch .LBB0_1506
